# C2 scan: each step's inputs requested one step ahead (two register sets, unrolled); on top of the C1 counted-wait change
# speedup vs baseline: 1.0121x; 1.0036x over previous
; __device__ __forceinline__ unsigned cvt_pk_bf16(float lo, float hi) { const bf16x2_t r = __builtin_convertvector((f32x2_t){lo, hi}, bf16x2_t); return __builtin_bit_cast(unsigned, r); }
; __device__ __forceinline__ int tid_hidden() { int t = threadIdx.x; asm volatile("" : "+v"(t)); return t; }
; #define DEC WSP(float, W_DEC)
; __device__ __forceinline__ void c2_phase(const bf16_t* __restrict__ UT, const float* __restrict__ DEC, bf16_t* __restrict__ SIN, int G, int c) {
;     for (int w = c * 512 + tid_hidden(); w < 64 * 2048; w += G * 512) {
;         const int seq = w >> 11, e = (w >> 4) & 127, d8 = (w & 15) * 8, dir = seq >> 5;
;         float S[8];
; #pragma unroll
;         for (int k = 0; k < 8; ++k) S[k] = 0.f;
; #pragma unroll 4
;         for (int step = 0; step < 32; ++step) {
;             const int j = dir ? 31 - step : step;
;             const size_t idx = (size_t)seq * 32 + j;
;             const u32x4 u = __builtin_nontemporal_load((const u32x4*)(UT + idx * 16384 + e * 128 + d8));
;             const f32x4 dc0 = *(const f32x4*)(DEC + idx * 128 + d8), dc1 = *(const f32x4*)(DEC + idx * 128 + d8 + 4);
;             u32x4 o; o.x = cvt_pk_bf16(S[0], S[1]); o.y = cvt_pk_bf16(S[2], S[3]); o.z = cvt_pk_bf16(S[4], S[5]); o.w = cvt_pk_bf16(S[6], S[7]);
;             *(u32x4*)(SIN + idx * 16384 + e * 128 + d8) = o;
;             S[0] = dc0[0] * S[0] + __uint_as_float(u.x << 16); S[1] = dc0[1] * S[1] + __uint_as_float(u.x & 0xffff0000u);
;             S[2] = dc0[2] * S[2] + __uint_as_float(u.y << 16); S[3] = dc0[3] * S[3] + __uint_as_float(u.y & 0xffff0000u);
;             S[4] = dc1[0] * S[4] + __uint_as_float(u.z << 16); S[5] = dc1[1] * S[5] + __uint_as_float(u.z & 0xffff0000u);
;             S[6] = dc1[2] * S[6] + __uint_as_float(u.w << 16); S[7] = dc1[3] * S[7] + __uint_as_float(u.w & 0xffff0000u);
;         }
.LBB0_1025:
	v_lshlrev_b32_e32 v3, 3, v20
	v_lshlrev_b32_e32 v4, 4, v20
	v_and_b32_e32 v6, 0x78, v3
	v_and_b32_e32 v34, 0x7f00, v4
	v_ashrrev_i32_e32 v2, 11, v20
	v_lshl_add_u64 v[4:5], s[0:1], 0, v[34:35]
	v_lshlrev_b32_e32 v8, 1, v6
	v_mov_b32_e32 v9, v35
	v_lshl_add_u64 v[10:11], s[4:5], 0, v[34:35]
	s_mov_b32 s12, 0x10000
	v_ashrrev_i32_e32 v3, 31, v2
	v_lshl_add_u64 v[4:5], v[4:5], 0, v[8:9]
	v_lshlrev_b32_e32 v6, 2, v6
	v_mov_b32_e32 v7, v35
	v_lshl_add_u64 v[8:9], v[10:11], 0, v[8:9]
	v_mov_b32_e32 v10, 0
	v_cmp_gt_u32_e32 vcc, s12, v20
	v_lshlrev_b64 v[2:3], 5, v[2:3]
	v_lshl_add_u64 v[6:7], s[2:3], 0, v[6:7]
	s_mov_b32 s12, 0
	s_mov_b32 s13, 28
	v_mov_b32_e32 v11, v10
	v_mov_b32_e32 v18, v10
	v_mov_b32_e32 v19, v10
	v_mov_b32_e32 v12, v10
	v_mov_b32_e32 v13, v10
	v_mov_b32_e32 v14, v10
	v_mov_b32_e32 v15, v10
	v_mov_b32_e32 v107, 0
	v_mov_b32_e32 v40, 0
	v_mov_b32_e32 v41, 0
	v_mov_b32_e32 v42, 0
	v_mov_b32_e32 v43, 0
	v_mov_b32_e32 v44, 0
	v_mov_b32_e32 v45, 0
	v_mov_b32_e32 v46, 0
	v_mov_b32_e32 v47, 0
	v_mov_b32_e32 v106, 31
	v_cndmask_b32_e64 v106, v106, 0, vcc
	v_lshl_add_u64 v[108:109], v[2:3], 0, v[106:107]
	v_lshlrev_b64 v[110:111], 15, v[108:109]
	v_lshlrev_b64 v[108:109], 9, v[108:109]
	v_lshl_add_u64 v[112:113], v[4:5], 0, v[110:111]
	v_lshl_add_u64 v[108:109], v[6:7], 0, v[108:109]
	v_lshl_add_u64 v[96:97], v[8:9], 0, v[110:111]
	global_load_dwordx4 v[48:51], v[112:113], off nt
	global_load_dwordx4 v[52:55], v[108:109], off offset:16
	global_load_dwordx4 v[56:59], v[108:109], off
	v_mov_b32_e32 v106, 30
	v_cndmask_b32_e64 v106, v106, 1, vcc
	v_lshl_add_u64 v[108:109], v[2:3], 0, v[106:107]
	v_lshlrev_b64 v[110:111], 15, v[108:109]
	v_lshlrev_b64 v[108:109], 9, v[108:109]
	v_lshl_add_u64 v[112:113], v[4:5], 0, v[110:111]
	v_lshl_add_u64 v[108:109], v[6:7], 0, v[108:109]
	v_lshl_add_u64 v[98:99], v[8:9], 0, v[110:111]
	global_load_dwordx4 v[60:63], v[112:113], off nt
	global_load_dwordx4 v[64:67], v[108:109], off offset:16
	global_load_dwordx4 v[68:71], v[108:109], off
	v_cvt_pk_bf16_f32 v116, v40, v41
	v_cvt_pk_bf16_f32 v117, v42, v43
	v_cvt_pk_bf16_f32 v118, v44, v45
	v_cvt_pk_bf16_f32 v119, v46, v47
	global_store_dwordx4 v[96:97], v[116:119], off
	s_waitcnt vmcnt(4)
	v_lshlrev_b32_e32 v114, 16, v48
	v_and_b32_e32 v115, 0xffff0000, v48
	v_pk_fma_f32 v[40:41], v[40:41], v[56:57], v[114:115]
	v_lshlrev_b32_e32 v114, 16, v49
	v_and_b32_e32 v115, 0xffff0000, v49
	v_pk_fma_f32 v[42:43], v[42:43], v[58:59], v[114:115]
	v_lshlrev_b32_e32 v114, 16, v50
	v_and_b32_e32 v115, 0xffff0000, v50
	v_pk_fma_f32 v[44:45], v[44:45], v[52:53], v[114:115]
	v_lshlrev_b32_e32 v114, 16, v51
	v_and_b32_e32 v115, 0xffff0000, v51
	v_pk_fma_f32 v[46:47], v[46:47], v[54:55], v[114:115]
	v_mov_b32_e32 v106, 29
	v_cndmask_b32_e64 v106, v106, 2, vcc
	v_lshl_add_u64 v[108:109], v[2:3], 0, v[106:107]
	v_lshlrev_b64 v[110:111], 15, v[108:109]
	v_lshlrev_b64 v[108:109], 9, v[108:109]
	v_lshl_add_u64 v[112:113], v[4:5], 0, v[110:111]
	v_lshl_add_u64 v[108:109], v[6:7], 0, v[108:109]
	v_lshl_add_u64 v[96:97], v[8:9], 0, v[110:111]
	global_load_dwordx4 v[48:51], v[112:113], off nt
	global_load_dwordx4 v[52:55], v[108:109], off offset:16
	global_load_dwordx4 v[56:59], v[108:109], off
	v_cvt_pk_bf16_f32 v116, v40, v41
	v_cvt_pk_bf16_f32 v117, v42, v43
	v_cvt_pk_bf16_f32 v118, v44, v45
	v_cvt_pk_bf16_f32 v119, v46, v47
	global_store_dwordx4 v[98:99], v[116:119], off
	s_waitcnt vmcnt(5)
	v_lshlrev_b32_e32 v114, 16, v60
	v_and_b32_e32 v115, 0xffff0000, v60
	v_pk_fma_f32 v[40:41], v[40:41], v[68:69], v[114:115]
	v_lshlrev_b32_e32 v114, 16, v61
	v_and_b32_e32 v115, 0xffff0000, v61
	v_pk_fma_f32 v[42:43], v[42:43], v[70:71], v[114:115]
	v_lshlrev_b32_e32 v114, 16, v62
	v_and_b32_e32 v115, 0xffff0000, v62
	v_pk_fma_f32 v[44:45], v[44:45], v[64:65], v[114:115]
	v_lshlrev_b32_e32 v114, 16, v63
	v_and_b32_e32 v115, 0xffff0000, v63
	v_pk_fma_f32 v[46:47], v[46:47], v[66:67], v[114:115]
	v_mov_b32_e32 v106, 28
	v_cndmask_b32_e64 v106, v106, 3, vcc
	v_lshl_add_u64 v[108:109], v[2:3], 0, v[106:107]
	v_lshlrev_b64 v[110:111], 15, v[108:109]
	v_lshlrev_b64 v[108:109], 9, v[108:109]
	v_lshl_add_u64 v[112:113], v[4:5], 0, v[110:111]
	v_lshl_add_u64 v[108:109], v[6:7], 0, v[108:109]
	v_lshl_add_u64 v[98:99], v[8:9], 0, v[110:111]
	global_load_dwordx4 v[60:63], v[112:113], off nt
	global_load_dwordx4 v[64:67], v[108:109], off offset:16
	global_load_dwordx4 v[68:71], v[108:109], off
	v_cvt_pk_bf16_f32 v116, v40, v41
	v_cvt_pk_bf16_f32 v117, v42, v43
	v_cvt_pk_bf16_f32 v118, v44, v45
	v_cvt_pk_bf16_f32 v119, v46, v47
	global_store_dwordx4 v[96:97], v[116:119], off
	s_waitcnt vmcnt(5)
	v_lshlrev_b32_e32 v114, 16, v48
	v_and_b32_e32 v115, 0xffff0000, v48
	v_pk_fma_f32 v[40:41], v[40:41], v[56:57], v[114:115]
	v_lshlrev_b32_e32 v114, 16, v49
	v_and_b32_e32 v115, 0xffff0000, v49
	v_pk_fma_f32 v[42:43], v[42:43], v[58:59], v[114:115]
	v_lshlrev_b32_e32 v114, 16, v50
	v_and_b32_e32 v115, 0xffff0000, v50
	v_pk_fma_f32 v[44:45], v[44:45], v[52:53], v[114:115]
	v_lshlrev_b32_e32 v114, 16, v51
	v_and_b32_e32 v115, 0xffff0000, v51
	v_pk_fma_f32 v[46:47], v[46:47], v[54:55], v[114:115]
	v_mov_b32_e32 v106, 27
	v_cndmask_b32_e64 v106, v106, 4, vcc
	v_lshl_add_u64 v[108:109], v[2:3], 0, v[106:107]
	v_lshlrev_b64 v[110:111], 15, v[108:109]
	v_lshlrev_b64 v[108:109], 9, v[108:109]
	v_lshl_add_u64 v[112:113], v[4:5], 0, v[110:111]
	v_lshl_add_u64 v[108:109], v[6:7], 0, v[108:109]
	v_lshl_add_u64 v[96:97], v[8:9], 0, v[110:111]
	global_load_dwordx4 v[48:51], v[112:113], off nt
	global_load_dwordx4 v[52:55], v[108:109], off offset:16
	global_load_dwordx4 v[56:59], v[108:109], off
	v_cvt_pk_bf16_f32 v116, v40, v41
	v_cvt_pk_bf16_f32 v117, v42, v43
	v_cvt_pk_bf16_f32 v118, v44, v45
	v_cvt_pk_bf16_f32 v119, v46, v47
	global_store_dwordx4 v[98:99], v[116:119], off
	s_waitcnt vmcnt(5)
; __device__ __forceinline__ unsigned cvt_pk_bf16(float lo, float hi) { const bf16x2_t r = __builtin_convertvector((f32x2_t){lo, hi}, bf16x2_t); return __builtin_bit_cast(unsigned, r); }
; #define DEC WSP(float, W_DEC)
; __device__ __forceinline__ void c2_phase(const bf16_t* __restrict__ UT, const float* __restrict__ DEC, bf16_t* __restrict__ SIN, int G, int c) {
;     ...
;         for (int step = 0; step < 32; ++step) {
;             const int j = dir ? 31 - step : step;
;             const size_t idx = (size_t)seq * 32 + j;
;             const u32x4 u = __builtin_nontemporal_load((const u32x4*)(UT + idx * 16384 + e * 128 + d8));
;             const f32x4 dc0 = *(const f32x4*)(DEC + idx * 128 + d8), dc1 = *(const f32x4*)(DEC + idx * 128 + d8 + 4);
;             u32x4 o; o.x = cvt_pk_bf16(S[0], S[1]); o.y = cvt_pk_bf16(S[2], S[3]); o.z = cvt_pk_bf16(S[4], S[5]); o.w = cvt_pk_bf16(S[6], S[7]);
;             *(u32x4*)(SIN + idx * 16384 + e * 128 + d8) = o;
;             S[0] = dc0[0] * S[0] + __uint_as_float(u.x << 16); S[1] = dc0[1] * S[1] + __uint_as_float(u.x & 0xffff0000u);
;             S[2] = dc0[2] * S[2] + __uint_as_float(u.y << 16); S[3] = dc0[3] * S[3] + __uint_as_float(u.y & 0xffff0000u);
;             S[4] = dc1[0] * S[4] + __uint_as_float(u.z << 16); S[5] = dc1[1] * S[5] + __uint_as_float(u.z & 0xffff0000u);
;             S[6] = dc1[2] * S[6] + __uint_as_float(u.w << 16); S[7] = dc1[3] * S[7] + __uint_as_float(u.w & 0xffff0000u);
;         }
	v_lshlrev_b32_e32 v114, 16, v60
	v_and_b32_e32 v115, 0xffff0000, v60
	v_pk_fma_f32 v[40:41], v[40:41], v[68:69], v[114:115]
	v_lshlrev_b32_e32 v114, 16, v61
	v_and_b32_e32 v115, 0xffff0000, v61
	v_pk_fma_f32 v[42:43], v[42:43], v[70:71], v[114:115]
	v_lshlrev_b32_e32 v114, 16, v62
	v_and_b32_e32 v115, 0xffff0000, v62
	v_pk_fma_f32 v[44:45], v[44:45], v[64:65], v[114:115]
	v_lshlrev_b32_e32 v114, 16, v63
	v_and_b32_e32 v115, 0xffff0000, v63
	v_pk_fma_f32 v[46:47], v[46:47], v[66:67], v[114:115]
	v_mov_b32_e32 v106, 26
	v_cndmask_b32_e64 v106, v106, 5, vcc
	v_lshl_add_u64 v[108:109], v[2:3], 0, v[106:107]
	v_lshlrev_b64 v[110:111], 15, v[108:109]
	v_lshlrev_b64 v[108:109], 9, v[108:109]
	v_lshl_add_u64 v[112:113], v[4:5], 0, v[110:111]
	v_lshl_add_u64 v[108:109], v[6:7], 0, v[108:109]
	v_lshl_add_u64 v[98:99], v[8:9], 0, v[110:111]
	global_load_dwordx4 v[60:63], v[112:113], off nt
	global_load_dwordx4 v[64:67], v[108:109], off offset:16
	global_load_dwordx4 v[68:71], v[108:109], off
	v_cvt_pk_bf16_f32 v116, v40, v41
	v_cvt_pk_bf16_f32 v117, v42, v43
	v_cvt_pk_bf16_f32 v118, v44, v45
	v_cvt_pk_bf16_f32 v119, v46, v47
	global_store_dwordx4 v[96:97], v[116:119], off
	s_waitcnt vmcnt(5)
	v_lshlrev_b32_e32 v114, 16, v48
	v_and_b32_e32 v115, 0xffff0000, v48
	v_pk_fma_f32 v[40:41], v[40:41], v[56:57], v[114:115]
	v_lshlrev_b32_e32 v114, 16, v49
	v_and_b32_e32 v115, 0xffff0000, v49
	v_pk_fma_f32 v[42:43], v[42:43], v[58:59], v[114:115]
	v_lshlrev_b32_e32 v114, 16, v50
	v_and_b32_e32 v115, 0xffff0000, v50
	v_pk_fma_f32 v[44:45], v[44:45], v[52:53], v[114:115]
	v_lshlrev_b32_e32 v114, 16, v51
	v_and_b32_e32 v115, 0xffff0000, v51
	v_pk_fma_f32 v[46:47], v[46:47], v[54:55], v[114:115]
	v_mov_b32_e32 v106, 25
	v_cndmask_b32_e64 v106, v106, 6, vcc
	v_lshl_add_u64 v[108:109], v[2:3], 0, v[106:107]
	v_lshlrev_b64 v[110:111], 15, v[108:109]
	v_lshlrev_b64 v[108:109], 9, v[108:109]
	v_lshl_add_u64 v[112:113], v[4:5], 0, v[110:111]
	v_lshl_add_u64 v[108:109], v[6:7], 0, v[108:109]
	v_lshl_add_u64 v[96:97], v[8:9], 0, v[110:111]
	global_load_dwordx4 v[48:51], v[112:113], off nt
	global_load_dwordx4 v[52:55], v[108:109], off offset:16
	global_load_dwordx4 v[56:59], v[108:109], off
	v_cvt_pk_bf16_f32 v116, v40, v41
	v_cvt_pk_bf16_f32 v117, v42, v43
	v_cvt_pk_bf16_f32 v118, v44, v45
	v_cvt_pk_bf16_f32 v119, v46, v47
	global_store_dwordx4 v[98:99], v[116:119], off
	s_waitcnt vmcnt(5)
	v_lshlrev_b32_e32 v114, 16, v60
	v_and_b32_e32 v115, 0xffff0000, v60
	v_pk_fma_f32 v[40:41], v[40:41], v[68:69], v[114:115]
	v_lshlrev_b32_e32 v114, 16, v61
	v_and_b32_e32 v115, 0xffff0000, v61
	v_pk_fma_f32 v[42:43], v[42:43], v[70:71], v[114:115]
	v_lshlrev_b32_e32 v114, 16, v62
	v_and_b32_e32 v115, 0xffff0000, v62
	v_pk_fma_f32 v[44:45], v[44:45], v[64:65], v[114:115]
	v_lshlrev_b32_e32 v114, 16, v63
	v_and_b32_e32 v115, 0xffff0000, v63
	v_pk_fma_f32 v[46:47], v[46:47], v[66:67], v[114:115]
	v_mov_b32_e32 v106, 24
	v_cndmask_b32_e64 v106, v106, 7, vcc
	v_lshl_add_u64 v[108:109], v[2:3], 0, v[106:107]
	v_lshlrev_b64 v[110:111], 15, v[108:109]
	v_lshlrev_b64 v[108:109], 9, v[108:109]
	v_lshl_add_u64 v[112:113], v[4:5], 0, v[110:111]
	v_lshl_add_u64 v[108:109], v[6:7], 0, v[108:109]
	v_lshl_add_u64 v[98:99], v[8:9], 0, v[110:111]
	global_load_dwordx4 v[60:63], v[112:113], off nt
	global_load_dwordx4 v[64:67], v[108:109], off offset:16
	global_load_dwordx4 v[68:71], v[108:109], off
	v_cvt_pk_bf16_f32 v116, v40, v41
	v_cvt_pk_bf16_f32 v117, v42, v43
	v_cvt_pk_bf16_f32 v118, v44, v45
	v_cvt_pk_bf16_f32 v119, v46, v47
	global_store_dwordx4 v[96:97], v[116:119], off
	s_waitcnt vmcnt(5)
	v_lshlrev_b32_e32 v114, 16, v48
	v_and_b32_e32 v115, 0xffff0000, v48
	v_pk_fma_f32 v[40:41], v[40:41], v[56:57], v[114:115]
	v_lshlrev_b32_e32 v114, 16, v49
	v_and_b32_e32 v115, 0xffff0000, v49
	v_pk_fma_f32 v[42:43], v[42:43], v[58:59], v[114:115]
	v_lshlrev_b32_e32 v114, 16, v50
	v_and_b32_e32 v115, 0xffff0000, v50
	v_pk_fma_f32 v[44:45], v[44:45], v[52:53], v[114:115]
	v_lshlrev_b32_e32 v114, 16, v51
	v_and_b32_e32 v115, 0xffff0000, v51
	v_pk_fma_f32 v[46:47], v[46:47], v[54:55], v[114:115]
	v_mov_b32_e32 v106, 23
	v_cndmask_b32_e64 v106, v106, 8, vcc
	v_lshl_add_u64 v[108:109], v[2:3], 0, v[106:107]
	v_lshlrev_b64 v[110:111], 15, v[108:109]
	v_lshlrev_b64 v[108:109], 9, v[108:109]
	v_lshl_add_u64 v[112:113], v[4:5], 0, v[110:111]
	v_lshl_add_u64 v[108:109], v[6:7], 0, v[108:109]
	v_lshl_add_u64 v[96:97], v[8:9], 0, v[110:111]
	global_load_dwordx4 v[48:51], v[112:113], off nt
	global_load_dwordx4 v[52:55], v[108:109], off offset:16
	global_load_dwordx4 v[56:59], v[108:109], off
	v_cvt_pk_bf16_f32 v116, v40, v41
	v_cvt_pk_bf16_f32 v117, v42, v43
	v_cvt_pk_bf16_f32 v118, v44, v45
	v_cvt_pk_bf16_f32 v119, v46, v47
	global_store_dwordx4 v[98:99], v[116:119], off
	s_waitcnt vmcnt(5)
	v_lshlrev_b32_e32 v114, 16, v60
	v_and_b32_e32 v115, 0xffff0000, v60
	v_pk_fma_f32 v[40:41], v[40:41], v[68:69], v[114:115]
	v_lshlrev_b32_e32 v114, 16, v61
	v_and_b32_e32 v115, 0xffff0000, v61
	v_pk_fma_f32 v[42:43], v[42:43], v[70:71], v[114:115]
	v_lshlrev_b32_e32 v114, 16, v62
	v_and_b32_e32 v115, 0xffff0000, v62
	v_pk_fma_f32 v[44:45], v[44:45], v[64:65], v[114:115]
	v_lshlrev_b32_e32 v114, 16, v63
	v_and_b32_e32 v115, 0xffff0000, v63
	v_pk_fma_f32 v[46:47], v[46:47], v[66:67], v[114:115]
	v_mov_b32_e32 v106, 22
	v_cndmask_b32_e64 v106, v106, 9, vcc
	v_lshl_add_u64 v[108:109], v[2:3], 0, v[106:107]
	v_lshlrev_b64 v[110:111], 15, v[108:109]
	v_lshlrev_b64 v[108:109], 9, v[108:109]
	v_lshl_add_u64 v[112:113], v[4:5], 0, v[110:111]
	v_lshl_add_u64 v[108:109], v[6:7], 0, v[108:109]
	v_lshl_add_u64 v[98:99], v[8:9], 0, v[110:111]
	global_load_dwordx4 v[60:63], v[112:113], off nt
	global_load_dwordx4 v[64:67], v[108:109], off offset:16
	global_load_dwordx4 v[68:71], v[108:109], off
	v_cvt_pk_bf16_f32 v116, v40, v41
	v_cvt_pk_bf16_f32 v117, v42, v43
	v_cvt_pk_bf16_f32 v118, v44, v45
	v_cvt_pk_bf16_f32 v119, v46, v47
	global_store_dwordx4 v[96:97], v[116:119], off
	s_waitcnt vmcnt(5)
; __device__ __forceinline__ unsigned cvt_pk_bf16(float lo, float hi) { const bf16x2_t r = __builtin_convertvector((f32x2_t){lo, hi}, bf16x2_t); return __builtin_bit_cast(unsigned, r); }
; #define DEC WSP(float, W_DEC)
; __device__ __forceinline__ void c2_phase(const bf16_t* __restrict__ UT, const float* __restrict__ DEC, bf16_t* __restrict__ SIN, int G, int c) {
;     ...
;         for (int step = 0; step < 32; ++step) {
;             const int j = dir ? 31 - step : step;
;             const size_t idx = (size_t)seq * 32 + j;
;             const u32x4 u = __builtin_nontemporal_load((const u32x4*)(UT + idx * 16384 + e * 128 + d8));
;             const f32x4 dc0 = *(const f32x4*)(DEC + idx * 128 + d8), dc1 = *(const f32x4*)(DEC + idx * 128 + d8 + 4);
;             u32x4 o; o.x = cvt_pk_bf16(S[0], S[1]); o.y = cvt_pk_bf16(S[2], S[3]); o.z = cvt_pk_bf16(S[4], S[5]); o.w = cvt_pk_bf16(S[6], S[7]);
;             *(u32x4*)(SIN + idx * 16384 + e * 128 + d8) = o;
;             S[0] = dc0[0] * S[0] + __uint_as_float(u.x << 16); S[1] = dc0[1] * S[1] + __uint_as_float(u.x & 0xffff0000u);
;             S[2] = dc0[2] * S[2] + __uint_as_float(u.y << 16); S[3] = dc0[3] * S[3] + __uint_as_float(u.y & 0xffff0000u);
;             S[4] = dc1[0] * S[4] + __uint_as_float(u.z << 16); S[5] = dc1[1] * S[5] + __uint_as_float(u.z & 0xffff0000u);
;             S[6] = dc1[2] * S[6] + __uint_as_float(u.w << 16); S[7] = dc1[3] * S[7] + __uint_as_float(u.w & 0xffff0000u);
;         }
	v_lshlrev_b32_e32 v114, 16, v48
	v_and_b32_e32 v115, 0xffff0000, v48
	v_pk_fma_f32 v[40:41], v[40:41], v[56:57], v[114:115]
	v_lshlrev_b32_e32 v114, 16, v49
	v_and_b32_e32 v115, 0xffff0000, v49
	v_pk_fma_f32 v[42:43], v[42:43], v[58:59], v[114:115]
	v_lshlrev_b32_e32 v114, 16, v50
	v_and_b32_e32 v115, 0xffff0000, v50
	v_pk_fma_f32 v[44:45], v[44:45], v[52:53], v[114:115]
	v_lshlrev_b32_e32 v114, 16, v51
	v_and_b32_e32 v115, 0xffff0000, v51
	v_pk_fma_f32 v[46:47], v[46:47], v[54:55], v[114:115]
	v_mov_b32_e32 v106, 21
	v_cndmask_b32_e64 v106, v106, 10, vcc
	v_lshl_add_u64 v[108:109], v[2:3], 0, v[106:107]
	v_lshlrev_b64 v[110:111], 15, v[108:109]
	v_lshlrev_b64 v[108:109], 9, v[108:109]
	v_lshl_add_u64 v[112:113], v[4:5], 0, v[110:111]
	v_lshl_add_u64 v[108:109], v[6:7], 0, v[108:109]
	v_lshl_add_u64 v[96:97], v[8:9], 0, v[110:111]
	global_load_dwordx4 v[48:51], v[112:113], off nt
	global_load_dwordx4 v[52:55], v[108:109], off offset:16
	global_load_dwordx4 v[56:59], v[108:109], off
	v_cvt_pk_bf16_f32 v116, v40, v41
	v_cvt_pk_bf16_f32 v117, v42, v43
	v_cvt_pk_bf16_f32 v118, v44, v45
	v_cvt_pk_bf16_f32 v119, v46, v47
	global_store_dwordx4 v[98:99], v[116:119], off
	s_waitcnt vmcnt(5)
	v_lshlrev_b32_e32 v114, 16, v60
	v_and_b32_e32 v115, 0xffff0000, v60
	v_pk_fma_f32 v[40:41], v[40:41], v[68:69], v[114:115]
	v_lshlrev_b32_e32 v114, 16, v61
	v_and_b32_e32 v115, 0xffff0000, v61
	v_pk_fma_f32 v[42:43], v[42:43], v[70:71], v[114:115]
	v_lshlrev_b32_e32 v114, 16, v62
	v_and_b32_e32 v115, 0xffff0000, v62
	v_pk_fma_f32 v[44:45], v[44:45], v[64:65], v[114:115]
	v_lshlrev_b32_e32 v114, 16, v63
	v_and_b32_e32 v115, 0xffff0000, v63
	v_pk_fma_f32 v[46:47], v[46:47], v[66:67], v[114:115]
	v_mov_b32_e32 v106, 20
	v_cndmask_b32_e64 v106, v106, 11, vcc
	v_lshl_add_u64 v[108:109], v[2:3], 0, v[106:107]
	v_lshlrev_b64 v[110:111], 15, v[108:109]
	v_lshlrev_b64 v[108:109], 9, v[108:109]
	v_lshl_add_u64 v[112:113], v[4:5], 0, v[110:111]
	v_lshl_add_u64 v[108:109], v[6:7], 0, v[108:109]
	v_lshl_add_u64 v[98:99], v[8:9], 0, v[110:111]
	global_load_dwordx4 v[60:63], v[112:113], off nt
	global_load_dwordx4 v[64:67], v[108:109], off offset:16
	global_load_dwordx4 v[68:71], v[108:109], off
	v_cvt_pk_bf16_f32 v116, v40, v41
	v_cvt_pk_bf16_f32 v117, v42, v43
	v_cvt_pk_bf16_f32 v118, v44, v45
	v_cvt_pk_bf16_f32 v119, v46, v47
	global_store_dwordx4 v[96:97], v[116:119], off
	s_waitcnt vmcnt(5)
	v_lshlrev_b32_e32 v114, 16, v48
	v_and_b32_e32 v115, 0xffff0000, v48
	v_pk_fma_f32 v[40:41], v[40:41], v[56:57], v[114:115]
	v_lshlrev_b32_e32 v114, 16, v49
	v_and_b32_e32 v115, 0xffff0000, v49
	v_pk_fma_f32 v[42:43], v[42:43], v[58:59], v[114:115]
	v_lshlrev_b32_e32 v114, 16, v50
	v_and_b32_e32 v115, 0xffff0000, v50
	v_pk_fma_f32 v[44:45], v[44:45], v[52:53], v[114:115]
	v_lshlrev_b32_e32 v114, 16, v51
	v_and_b32_e32 v115, 0xffff0000, v51
	v_pk_fma_f32 v[46:47], v[46:47], v[54:55], v[114:115]
	v_mov_b32_e32 v106, 19
	v_cndmask_b32_e64 v106, v106, 12, vcc
	v_lshl_add_u64 v[108:109], v[2:3], 0, v[106:107]
	v_lshlrev_b64 v[110:111], 15, v[108:109]
	v_lshlrev_b64 v[108:109], 9, v[108:109]
	v_lshl_add_u64 v[112:113], v[4:5], 0, v[110:111]
	v_lshl_add_u64 v[108:109], v[6:7], 0, v[108:109]
	v_lshl_add_u64 v[96:97], v[8:9], 0, v[110:111]
	global_load_dwordx4 v[48:51], v[112:113], off nt
	global_load_dwordx4 v[52:55], v[108:109], off offset:16
	global_load_dwordx4 v[56:59], v[108:109], off
	v_cvt_pk_bf16_f32 v116, v40, v41
	v_cvt_pk_bf16_f32 v117, v42, v43
	v_cvt_pk_bf16_f32 v118, v44, v45
	v_cvt_pk_bf16_f32 v119, v46, v47
	global_store_dwordx4 v[98:99], v[116:119], off
	s_waitcnt vmcnt(5)
	v_lshlrev_b32_e32 v114, 16, v60
	v_and_b32_e32 v115, 0xffff0000, v60
	v_pk_fma_f32 v[40:41], v[40:41], v[68:69], v[114:115]
	v_lshlrev_b32_e32 v114, 16, v61
	v_and_b32_e32 v115, 0xffff0000, v61
	v_pk_fma_f32 v[42:43], v[42:43], v[70:71], v[114:115]
	v_lshlrev_b32_e32 v114, 16, v62
	v_and_b32_e32 v115, 0xffff0000, v62
	v_pk_fma_f32 v[44:45], v[44:45], v[64:65], v[114:115]
	v_lshlrev_b32_e32 v114, 16, v63
	v_and_b32_e32 v115, 0xffff0000, v63
	v_pk_fma_f32 v[46:47], v[46:47], v[66:67], v[114:115]
	v_mov_b32_e32 v106, 18
	v_cndmask_b32_e64 v106, v106, 13, vcc
	v_lshl_add_u64 v[108:109], v[2:3], 0, v[106:107]
	v_lshlrev_b64 v[110:111], 15, v[108:109]
	v_lshlrev_b64 v[108:109], 9, v[108:109]
	v_lshl_add_u64 v[112:113], v[4:5], 0, v[110:111]
	v_lshl_add_u64 v[108:109], v[6:7], 0, v[108:109]
	v_lshl_add_u64 v[98:99], v[8:9], 0, v[110:111]
	global_load_dwordx4 v[60:63], v[112:113], off nt
	global_load_dwordx4 v[64:67], v[108:109], off offset:16
	global_load_dwordx4 v[68:71], v[108:109], off
	v_cvt_pk_bf16_f32 v116, v40, v41
	v_cvt_pk_bf16_f32 v117, v42, v43
	v_cvt_pk_bf16_f32 v118, v44, v45
	v_cvt_pk_bf16_f32 v119, v46, v47
	global_store_dwordx4 v[96:97], v[116:119], off
	s_waitcnt vmcnt(5)
	v_lshlrev_b32_e32 v114, 16, v48
	v_and_b32_e32 v115, 0xffff0000, v48
	v_pk_fma_f32 v[40:41], v[40:41], v[56:57], v[114:115]
	v_lshlrev_b32_e32 v114, 16, v49
	v_and_b32_e32 v115, 0xffff0000, v49
	v_pk_fma_f32 v[42:43], v[42:43], v[58:59], v[114:115]
	v_lshlrev_b32_e32 v114, 16, v50
	v_and_b32_e32 v115, 0xffff0000, v50
	v_pk_fma_f32 v[44:45], v[44:45], v[52:53], v[114:115]
	v_lshlrev_b32_e32 v114, 16, v51
	v_and_b32_e32 v115, 0xffff0000, v51
	v_pk_fma_f32 v[46:47], v[46:47], v[54:55], v[114:115]
	v_mov_b32_e32 v106, 17
	v_cndmask_b32_e64 v106, v106, 14, vcc
	v_lshl_add_u64 v[108:109], v[2:3], 0, v[106:107]
	v_lshlrev_b64 v[110:111], 15, v[108:109]
	v_lshlrev_b64 v[108:109], 9, v[108:109]
	v_lshl_add_u64 v[112:113], v[4:5], 0, v[110:111]
	v_lshl_add_u64 v[108:109], v[6:7], 0, v[108:109]
	v_lshl_add_u64 v[96:97], v[8:9], 0, v[110:111]
	global_load_dwordx4 v[48:51], v[112:113], off nt
	global_load_dwordx4 v[52:55], v[108:109], off offset:16
	global_load_dwordx4 v[56:59], v[108:109], off
	v_cvt_pk_bf16_f32 v116, v40, v41
	v_cvt_pk_bf16_f32 v117, v42, v43
	v_cvt_pk_bf16_f32 v118, v44, v45
	v_cvt_pk_bf16_f32 v119, v46, v47
	global_store_dwordx4 v[98:99], v[116:119], off
	s_waitcnt vmcnt(5)
; __device__ __forceinline__ unsigned cvt_pk_bf16(float lo, float hi) { const bf16x2_t r = __builtin_convertvector((f32x2_t){lo, hi}, bf16x2_t); return __builtin_bit_cast(unsigned, r); }
; #define DEC WSP(float, W_DEC)
; __device__ __forceinline__ void c2_phase(const bf16_t* __restrict__ UT, const float* __restrict__ DEC, bf16_t* __restrict__ SIN, int G, int c) {
;     ...
;         for (int step = 0; step < 32; ++step) {
;             const int j = dir ? 31 - step : step;
;             const size_t idx = (size_t)seq * 32 + j;
;             const u32x4 u = __builtin_nontemporal_load((const u32x4*)(UT + idx * 16384 + e * 128 + d8));
;             const f32x4 dc0 = *(const f32x4*)(DEC + idx * 128 + d8), dc1 = *(const f32x4*)(DEC + idx * 128 + d8 + 4);
;             u32x4 o; o.x = cvt_pk_bf16(S[0], S[1]); o.y = cvt_pk_bf16(S[2], S[3]); o.z = cvt_pk_bf16(S[4], S[5]); o.w = cvt_pk_bf16(S[6], S[7]);
;             *(u32x4*)(SIN + idx * 16384 + e * 128 + d8) = o;
;             S[0] = dc0[0] * S[0] + __uint_as_float(u.x << 16); S[1] = dc0[1] * S[1] + __uint_as_float(u.x & 0xffff0000u);
;             S[2] = dc0[2] * S[2] + __uint_as_float(u.y << 16); S[3] = dc0[3] * S[3] + __uint_as_float(u.y & 0xffff0000u);
;             S[4] = dc1[0] * S[4] + __uint_as_float(u.z << 16); S[5] = dc1[1] * S[5] + __uint_as_float(u.z & 0xffff0000u);
;             S[6] = dc1[2] * S[6] + __uint_as_float(u.w << 16); S[7] = dc1[3] * S[7] + __uint_as_float(u.w & 0xffff0000u);
;         }
	v_lshlrev_b32_e32 v114, 16, v60
	v_and_b32_e32 v115, 0xffff0000, v60
	v_pk_fma_f32 v[40:41], v[40:41], v[68:69], v[114:115]
	v_lshlrev_b32_e32 v114, 16, v61
	v_and_b32_e32 v115, 0xffff0000, v61
	v_pk_fma_f32 v[42:43], v[42:43], v[70:71], v[114:115]
	v_lshlrev_b32_e32 v114, 16, v62
	v_and_b32_e32 v115, 0xffff0000, v62
	v_pk_fma_f32 v[44:45], v[44:45], v[64:65], v[114:115]
	v_lshlrev_b32_e32 v114, 16, v63
	v_and_b32_e32 v115, 0xffff0000, v63
	v_pk_fma_f32 v[46:47], v[46:47], v[66:67], v[114:115]
	v_mov_b32_e32 v106, 16
	v_cndmask_b32_e64 v106, v106, 15, vcc
	v_lshl_add_u64 v[108:109], v[2:3], 0, v[106:107]
	v_lshlrev_b64 v[110:111], 15, v[108:109]
	v_lshlrev_b64 v[108:109], 9, v[108:109]
	v_lshl_add_u64 v[112:113], v[4:5], 0, v[110:111]
	v_lshl_add_u64 v[108:109], v[6:7], 0, v[108:109]
	v_lshl_add_u64 v[98:99], v[8:9], 0, v[110:111]
	global_load_dwordx4 v[60:63], v[112:113], off nt
	global_load_dwordx4 v[64:67], v[108:109], off offset:16
	global_load_dwordx4 v[68:71], v[108:109], off
	v_cvt_pk_bf16_f32 v116, v40, v41
	v_cvt_pk_bf16_f32 v117, v42, v43
	v_cvt_pk_bf16_f32 v118, v44, v45
	v_cvt_pk_bf16_f32 v119, v46, v47
	global_store_dwordx4 v[96:97], v[116:119], off
	s_waitcnt vmcnt(5)
	v_lshlrev_b32_e32 v114, 16, v48
	v_and_b32_e32 v115, 0xffff0000, v48
	v_pk_fma_f32 v[40:41], v[40:41], v[56:57], v[114:115]
	v_lshlrev_b32_e32 v114, 16, v49
	v_and_b32_e32 v115, 0xffff0000, v49
	v_pk_fma_f32 v[42:43], v[42:43], v[58:59], v[114:115]
	v_lshlrev_b32_e32 v114, 16, v50
	v_and_b32_e32 v115, 0xffff0000, v50
	v_pk_fma_f32 v[44:45], v[44:45], v[52:53], v[114:115]
	v_lshlrev_b32_e32 v114, 16, v51
	v_and_b32_e32 v115, 0xffff0000, v51
	v_pk_fma_f32 v[46:47], v[46:47], v[54:55], v[114:115]
	v_mov_b32_e32 v106, 15
	v_cndmask_b32_e64 v106, v106, 16, vcc
	v_lshl_add_u64 v[108:109], v[2:3], 0, v[106:107]
	v_lshlrev_b64 v[110:111], 15, v[108:109]
	v_lshlrev_b64 v[108:109], 9, v[108:109]
	v_lshl_add_u64 v[112:113], v[4:5], 0, v[110:111]
	v_lshl_add_u64 v[108:109], v[6:7], 0, v[108:109]
	v_lshl_add_u64 v[96:97], v[8:9], 0, v[110:111]
	global_load_dwordx4 v[48:51], v[112:113], off nt
	global_load_dwordx4 v[52:55], v[108:109], off offset:16
	global_load_dwordx4 v[56:59], v[108:109], off
	v_cvt_pk_bf16_f32 v116, v40, v41
	v_cvt_pk_bf16_f32 v117, v42, v43
	v_cvt_pk_bf16_f32 v118, v44, v45
	v_cvt_pk_bf16_f32 v119, v46, v47
	global_store_dwordx4 v[98:99], v[116:119], off
	s_waitcnt vmcnt(5)
	v_lshlrev_b32_e32 v114, 16, v60
	v_and_b32_e32 v115, 0xffff0000, v60
	v_pk_fma_f32 v[40:41], v[40:41], v[68:69], v[114:115]
	v_lshlrev_b32_e32 v114, 16, v61
	v_and_b32_e32 v115, 0xffff0000, v61
	v_pk_fma_f32 v[42:43], v[42:43], v[70:71], v[114:115]
	v_lshlrev_b32_e32 v114, 16, v62
	v_and_b32_e32 v115, 0xffff0000, v62
	v_pk_fma_f32 v[44:45], v[44:45], v[64:65], v[114:115]
	v_lshlrev_b32_e32 v114, 16, v63
	v_and_b32_e32 v115, 0xffff0000, v63
	v_pk_fma_f32 v[46:47], v[46:47], v[66:67], v[114:115]
	v_mov_b32_e32 v106, 14
	v_cndmask_b32_e64 v106, v106, 17, vcc
	v_lshl_add_u64 v[108:109], v[2:3], 0, v[106:107]
	v_lshlrev_b64 v[110:111], 15, v[108:109]
	v_lshlrev_b64 v[108:109], 9, v[108:109]
	v_lshl_add_u64 v[112:113], v[4:5], 0, v[110:111]
	v_lshl_add_u64 v[108:109], v[6:7], 0, v[108:109]
	v_lshl_add_u64 v[98:99], v[8:9], 0, v[110:111]
	global_load_dwordx4 v[60:63], v[112:113], off nt
	global_load_dwordx4 v[64:67], v[108:109], off offset:16
	global_load_dwordx4 v[68:71], v[108:109], off
	v_cvt_pk_bf16_f32 v116, v40, v41
	v_cvt_pk_bf16_f32 v117, v42, v43
	v_cvt_pk_bf16_f32 v118, v44, v45
	v_cvt_pk_bf16_f32 v119, v46, v47
	global_store_dwordx4 v[96:97], v[116:119], off
	s_waitcnt vmcnt(5)
	v_lshlrev_b32_e32 v114, 16, v48
	v_and_b32_e32 v115, 0xffff0000, v48
	v_pk_fma_f32 v[40:41], v[40:41], v[56:57], v[114:115]
	v_lshlrev_b32_e32 v114, 16, v49
	v_and_b32_e32 v115, 0xffff0000, v49
	v_pk_fma_f32 v[42:43], v[42:43], v[58:59], v[114:115]
	v_lshlrev_b32_e32 v114, 16, v50
	v_and_b32_e32 v115, 0xffff0000, v50
	v_pk_fma_f32 v[44:45], v[44:45], v[52:53], v[114:115]
	v_lshlrev_b32_e32 v114, 16, v51
	v_and_b32_e32 v115, 0xffff0000, v51
	v_pk_fma_f32 v[46:47], v[46:47], v[54:55], v[114:115]
	v_mov_b32_e32 v106, 13
	v_cndmask_b32_e64 v106, v106, 18, vcc
	v_lshl_add_u64 v[108:109], v[2:3], 0, v[106:107]
	v_lshlrev_b64 v[110:111], 15, v[108:109]
	v_lshlrev_b64 v[108:109], 9, v[108:109]
	v_lshl_add_u64 v[112:113], v[4:5], 0, v[110:111]
	v_lshl_add_u64 v[108:109], v[6:7], 0, v[108:109]
	v_lshl_add_u64 v[96:97], v[8:9], 0, v[110:111]
	global_load_dwordx4 v[48:51], v[112:113], off nt
	global_load_dwordx4 v[52:55], v[108:109], off offset:16
	global_load_dwordx4 v[56:59], v[108:109], off
	v_cvt_pk_bf16_f32 v116, v40, v41
	v_cvt_pk_bf16_f32 v117, v42, v43
	v_cvt_pk_bf16_f32 v118, v44, v45
	v_cvt_pk_bf16_f32 v119, v46, v47
	global_store_dwordx4 v[98:99], v[116:119], off
	s_waitcnt vmcnt(5)
	v_lshlrev_b32_e32 v114, 16, v60
	v_and_b32_e32 v115, 0xffff0000, v60
	v_pk_fma_f32 v[40:41], v[40:41], v[68:69], v[114:115]
	v_lshlrev_b32_e32 v114, 16, v61
	v_and_b32_e32 v115, 0xffff0000, v61
	v_pk_fma_f32 v[42:43], v[42:43], v[70:71], v[114:115]
	v_lshlrev_b32_e32 v114, 16, v62
	v_and_b32_e32 v115, 0xffff0000, v62
	v_pk_fma_f32 v[44:45], v[44:45], v[64:65], v[114:115]
	v_lshlrev_b32_e32 v114, 16, v63
	v_and_b32_e32 v115, 0xffff0000, v63
	v_pk_fma_f32 v[46:47], v[46:47], v[66:67], v[114:115]
	v_mov_b32_e32 v106, 12
	v_cndmask_b32_e64 v106, v106, 19, vcc
	v_lshl_add_u64 v[108:109], v[2:3], 0, v[106:107]
	v_lshlrev_b64 v[110:111], 15, v[108:109]
	v_lshlrev_b64 v[108:109], 9, v[108:109]
	v_lshl_add_u64 v[112:113], v[4:5], 0, v[110:111]
	v_lshl_add_u64 v[108:109], v[6:7], 0, v[108:109]
	v_lshl_add_u64 v[98:99], v[8:9], 0, v[110:111]
	global_load_dwordx4 v[60:63], v[112:113], off nt
	global_load_dwordx4 v[64:67], v[108:109], off offset:16
	global_load_dwordx4 v[68:71], v[108:109], off
	v_cvt_pk_bf16_f32 v116, v40, v41
	v_cvt_pk_bf16_f32 v117, v42, v43
	v_cvt_pk_bf16_f32 v118, v44, v45
	v_cvt_pk_bf16_f32 v119, v46, v47
	global_store_dwordx4 v[96:97], v[116:119], off
	s_waitcnt vmcnt(5)
; __device__ __forceinline__ unsigned cvt_pk_bf16(float lo, float hi) { const bf16x2_t r = __builtin_convertvector((f32x2_t){lo, hi}, bf16x2_t); return __builtin_bit_cast(unsigned, r); }
; #define DEC WSP(float, W_DEC)
; __device__ __forceinline__ void c2_phase(const bf16_t* __restrict__ UT, const float* __restrict__ DEC, bf16_t* __restrict__ SIN, int G, int c) {
;     ...
;         for (int step = 0; step < 32; ++step) {
;             const int j = dir ? 31 - step : step;
;             const size_t idx = (size_t)seq * 32 + j;
;             const u32x4 u = __builtin_nontemporal_load((const u32x4*)(UT + idx * 16384 + e * 128 + d8));
;             const f32x4 dc0 = *(const f32x4*)(DEC + idx * 128 + d8), dc1 = *(const f32x4*)(DEC + idx * 128 + d8 + 4);
;             u32x4 o; o.x = cvt_pk_bf16(S[0], S[1]); o.y = cvt_pk_bf16(S[2], S[3]); o.z = cvt_pk_bf16(S[4], S[5]); o.w = cvt_pk_bf16(S[6], S[7]);
;             *(u32x4*)(SIN + idx * 16384 + e * 128 + d8) = o;
;             S[0] = dc0[0] * S[0] + __uint_as_float(u.x << 16); S[1] = dc0[1] * S[1] + __uint_as_float(u.x & 0xffff0000u);
;             S[2] = dc0[2] * S[2] + __uint_as_float(u.y << 16); S[3] = dc0[3] * S[3] + __uint_as_float(u.y & 0xffff0000u);
;             S[4] = dc1[0] * S[4] + __uint_as_float(u.z << 16); S[5] = dc1[1] * S[5] + __uint_as_float(u.z & 0xffff0000u);
;             S[6] = dc1[2] * S[6] + __uint_as_float(u.w << 16); S[7] = dc1[3] * S[7] + __uint_as_float(u.w & 0xffff0000u);
;         }
	v_lshlrev_b32_e32 v114, 16, v48
	v_and_b32_e32 v115, 0xffff0000, v48
	v_pk_fma_f32 v[40:41], v[40:41], v[56:57], v[114:115]
	v_lshlrev_b32_e32 v114, 16, v49
	v_and_b32_e32 v115, 0xffff0000, v49
	v_pk_fma_f32 v[42:43], v[42:43], v[58:59], v[114:115]
	v_lshlrev_b32_e32 v114, 16, v50
	v_and_b32_e32 v115, 0xffff0000, v50
	v_pk_fma_f32 v[44:45], v[44:45], v[52:53], v[114:115]
	v_lshlrev_b32_e32 v114, 16, v51
	v_and_b32_e32 v115, 0xffff0000, v51
	v_pk_fma_f32 v[46:47], v[46:47], v[54:55], v[114:115]
	v_mov_b32_e32 v106, 11
	v_cndmask_b32_e64 v106, v106, 20, vcc
	v_lshl_add_u64 v[108:109], v[2:3], 0, v[106:107]
	v_lshlrev_b64 v[110:111], 15, v[108:109]
	v_lshlrev_b64 v[108:109], 9, v[108:109]
	v_lshl_add_u64 v[112:113], v[4:5], 0, v[110:111]
	v_lshl_add_u64 v[108:109], v[6:7], 0, v[108:109]
	v_lshl_add_u64 v[96:97], v[8:9], 0, v[110:111]
	global_load_dwordx4 v[48:51], v[112:113], off nt
	global_load_dwordx4 v[52:55], v[108:109], off offset:16
	global_load_dwordx4 v[56:59], v[108:109], off
	v_cvt_pk_bf16_f32 v116, v40, v41
	v_cvt_pk_bf16_f32 v117, v42, v43
	v_cvt_pk_bf16_f32 v118, v44, v45
	v_cvt_pk_bf16_f32 v119, v46, v47
	global_store_dwordx4 v[98:99], v[116:119], off
	s_waitcnt vmcnt(5)
	v_lshlrev_b32_e32 v114, 16, v60
	v_and_b32_e32 v115, 0xffff0000, v60
	v_pk_fma_f32 v[40:41], v[40:41], v[68:69], v[114:115]
	v_lshlrev_b32_e32 v114, 16, v61
	v_and_b32_e32 v115, 0xffff0000, v61
	v_pk_fma_f32 v[42:43], v[42:43], v[70:71], v[114:115]
	v_lshlrev_b32_e32 v114, 16, v62
	v_and_b32_e32 v115, 0xffff0000, v62
	v_pk_fma_f32 v[44:45], v[44:45], v[64:65], v[114:115]
	v_lshlrev_b32_e32 v114, 16, v63
	v_and_b32_e32 v115, 0xffff0000, v63
	v_pk_fma_f32 v[46:47], v[46:47], v[66:67], v[114:115]
	v_mov_b32_e32 v106, 10
	v_cndmask_b32_e64 v106, v106, 21, vcc
	v_lshl_add_u64 v[108:109], v[2:3], 0, v[106:107]
	v_lshlrev_b64 v[110:111], 15, v[108:109]
	v_lshlrev_b64 v[108:109], 9, v[108:109]
	v_lshl_add_u64 v[112:113], v[4:5], 0, v[110:111]
	v_lshl_add_u64 v[108:109], v[6:7], 0, v[108:109]
	v_lshl_add_u64 v[98:99], v[8:9], 0, v[110:111]
	global_load_dwordx4 v[60:63], v[112:113], off nt
	global_load_dwordx4 v[64:67], v[108:109], off offset:16
	global_load_dwordx4 v[68:71], v[108:109], off
	v_cvt_pk_bf16_f32 v116, v40, v41
	v_cvt_pk_bf16_f32 v117, v42, v43
	v_cvt_pk_bf16_f32 v118, v44, v45
	v_cvt_pk_bf16_f32 v119, v46, v47
	global_store_dwordx4 v[96:97], v[116:119], off
	s_waitcnt vmcnt(5)
	v_lshlrev_b32_e32 v114, 16, v48
	v_and_b32_e32 v115, 0xffff0000, v48
	v_pk_fma_f32 v[40:41], v[40:41], v[56:57], v[114:115]
	v_lshlrev_b32_e32 v114, 16, v49
	v_and_b32_e32 v115, 0xffff0000, v49
	v_pk_fma_f32 v[42:43], v[42:43], v[58:59], v[114:115]
	v_lshlrev_b32_e32 v114, 16, v50
	v_and_b32_e32 v115, 0xffff0000, v50
	v_pk_fma_f32 v[44:45], v[44:45], v[52:53], v[114:115]
	v_lshlrev_b32_e32 v114, 16, v51
	v_and_b32_e32 v115, 0xffff0000, v51
	v_pk_fma_f32 v[46:47], v[46:47], v[54:55], v[114:115]
	v_mov_b32_e32 v106, 9
	v_cndmask_b32_e64 v106, v106, 22, vcc
	v_lshl_add_u64 v[108:109], v[2:3], 0, v[106:107]
	v_lshlrev_b64 v[110:111], 15, v[108:109]
	v_lshlrev_b64 v[108:109], 9, v[108:109]
	v_lshl_add_u64 v[112:113], v[4:5], 0, v[110:111]
	v_lshl_add_u64 v[108:109], v[6:7], 0, v[108:109]
	v_lshl_add_u64 v[96:97], v[8:9], 0, v[110:111]
	global_load_dwordx4 v[48:51], v[112:113], off nt
	global_load_dwordx4 v[52:55], v[108:109], off offset:16
	global_load_dwordx4 v[56:59], v[108:109], off
	v_cvt_pk_bf16_f32 v116, v40, v41
	v_cvt_pk_bf16_f32 v117, v42, v43
	v_cvt_pk_bf16_f32 v118, v44, v45
	v_cvt_pk_bf16_f32 v119, v46, v47
	global_store_dwordx4 v[98:99], v[116:119], off
	s_waitcnt vmcnt(5)
	v_lshlrev_b32_e32 v114, 16, v60
	v_and_b32_e32 v115, 0xffff0000, v60
	v_pk_fma_f32 v[40:41], v[40:41], v[68:69], v[114:115]
	v_lshlrev_b32_e32 v114, 16, v61
	v_and_b32_e32 v115, 0xffff0000, v61
	v_pk_fma_f32 v[42:43], v[42:43], v[70:71], v[114:115]
	v_lshlrev_b32_e32 v114, 16, v62
	v_and_b32_e32 v115, 0xffff0000, v62
	v_pk_fma_f32 v[44:45], v[44:45], v[64:65], v[114:115]
	v_lshlrev_b32_e32 v114, 16, v63
	v_and_b32_e32 v115, 0xffff0000, v63
	v_pk_fma_f32 v[46:47], v[46:47], v[66:67], v[114:115]
	v_mov_b32_e32 v106, 8
	v_cndmask_b32_e64 v106, v106, 23, vcc
	v_lshl_add_u64 v[108:109], v[2:3], 0, v[106:107]
	v_lshlrev_b64 v[110:111], 15, v[108:109]
	v_lshlrev_b64 v[108:109], 9, v[108:109]
	v_lshl_add_u64 v[112:113], v[4:5], 0, v[110:111]
	v_lshl_add_u64 v[108:109], v[6:7], 0, v[108:109]
	v_lshl_add_u64 v[98:99], v[8:9], 0, v[110:111]
	global_load_dwordx4 v[60:63], v[112:113], off nt
	global_load_dwordx4 v[64:67], v[108:109], off offset:16
	global_load_dwordx4 v[68:71], v[108:109], off
	v_cvt_pk_bf16_f32 v116, v40, v41
	v_cvt_pk_bf16_f32 v117, v42, v43
	v_cvt_pk_bf16_f32 v118, v44, v45
	v_cvt_pk_bf16_f32 v119, v46, v47
	global_store_dwordx4 v[96:97], v[116:119], off
	s_waitcnt vmcnt(5)
	v_lshlrev_b32_e32 v114, 16, v48
	v_and_b32_e32 v115, 0xffff0000, v48
	v_pk_fma_f32 v[40:41], v[40:41], v[56:57], v[114:115]
	v_lshlrev_b32_e32 v114, 16, v49
	v_and_b32_e32 v115, 0xffff0000, v49
	v_pk_fma_f32 v[42:43], v[42:43], v[58:59], v[114:115]
	v_lshlrev_b32_e32 v114, 16, v50
	v_and_b32_e32 v115, 0xffff0000, v50
	v_pk_fma_f32 v[44:45], v[44:45], v[52:53], v[114:115]
	v_lshlrev_b32_e32 v114, 16, v51
	v_and_b32_e32 v115, 0xffff0000, v51
	v_pk_fma_f32 v[46:47], v[46:47], v[54:55], v[114:115]
	v_mov_b32_e32 v106, 7
	v_cndmask_b32_e64 v106, v106, 24, vcc
	v_lshl_add_u64 v[108:109], v[2:3], 0, v[106:107]
	v_lshlrev_b64 v[110:111], 15, v[108:109]
	v_lshlrev_b64 v[108:109], 9, v[108:109]
	v_lshl_add_u64 v[112:113], v[4:5], 0, v[110:111]
	v_lshl_add_u64 v[108:109], v[6:7], 0, v[108:109]
	v_lshl_add_u64 v[96:97], v[8:9], 0, v[110:111]
	global_load_dwordx4 v[48:51], v[112:113], off nt
	global_load_dwordx4 v[52:55], v[108:109], off offset:16
	global_load_dwordx4 v[56:59], v[108:109], off
	v_cvt_pk_bf16_f32 v116, v40, v41
	v_cvt_pk_bf16_f32 v117, v42, v43
	v_cvt_pk_bf16_f32 v118, v44, v45
	v_cvt_pk_bf16_f32 v119, v46, v47
	global_store_dwordx4 v[98:99], v[116:119], off
	s_waitcnt vmcnt(5)
; __device__ __forceinline__ unsigned cvt_pk_bf16(float lo, float hi) { const bf16x2_t r = __builtin_convertvector((f32x2_t){lo, hi}, bf16x2_t); return __builtin_bit_cast(unsigned, r); }
; #define DEC WSP(float, W_DEC)
; __device__ __forceinline__ void c2_phase(const bf16_t* __restrict__ UT, const float* __restrict__ DEC, bf16_t* __restrict__ SIN, int G, int c) {
;     ...
;         for (int step = 0; step < 32; ++step) {
;             const int j = dir ? 31 - step : step;
;             const size_t idx = (size_t)seq * 32 + j;
;             const u32x4 u = __builtin_nontemporal_load((const u32x4*)(UT + idx * 16384 + e * 128 + d8));
;             const f32x4 dc0 = *(const f32x4*)(DEC + idx * 128 + d8), dc1 = *(const f32x4*)(DEC + idx * 128 + d8 + 4);
;             u32x4 o; o.x = cvt_pk_bf16(S[0], S[1]); o.y = cvt_pk_bf16(S[2], S[3]); o.z = cvt_pk_bf16(S[4], S[5]); o.w = cvt_pk_bf16(S[6], S[7]);
;             *(u32x4*)(SIN + idx * 16384 + e * 128 + d8) = o;
;             S[0] = dc0[0] * S[0] + __uint_as_float(u.x << 16); S[1] = dc0[1] * S[1] + __uint_as_float(u.x & 0xffff0000u);
;             S[2] = dc0[2] * S[2] + __uint_as_float(u.y << 16); S[3] = dc0[3] * S[3] + __uint_as_float(u.y & 0xffff0000u);
;             S[4] = dc1[0] * S[4] + __uint_as_float(u.z << 16); S[5] = dc1[1] * S[5] + __uint_as_float(u.z & 0xffff0000u);
;             S[6] = dc1[2] * S[6] + __uint_as_float(u.w << 16); S[7] = dc1[3] * S[7] + __uint_as_float(u.w & 0xffff0000u);
;         }
	v_lshlrev_b32_e32 v114, 16, v60
	v_and_b32_e32 v115, 0xffff0000, v60
	v_pk_fma_f32 v[40:41], v[40:41], v[68:69], v[114:115]
	v_lshlrev_b32_e32 v114, 16, v61
	v_and_b32_e32 v115, 0xffff0000, v61
	v_pk_fma_f32 v[42:43], v[42:43], v[70:71], v[114:115]
	v_lshlrev_b32_e32 v114, 16, v62
	v_and_b32_e32 v115, 0xffff0000, v62
	v_pk_fma_f32 v[44:45], v[44:45], v[64:65], v[114:115]
	v_lshlrev_b32_e32 v114, 16, v63
	v_and_b32_e32 v115, 0xffff0000, v63
	v_pk_fma_f32 v[46:47], v[46:47], v[66:67], v[114:115]
	v_mov_b32_e32 v106, 6
	v_cndmask_b32_e64 v106, v106, 25, vcc
	v_lshl_add_u64 v[108:109], v[2:3], 0, v[106:107]
	v_lshlrev_b64 v[110:111], 15, v[108:109]
	v_lshlrev_b64 v[108:109], 9, v[108:109]
	v_lshl_add_u64 v[112:113], v[4:5], 0, v[110:111]
	v_lshl_add_u64 v[108:109], v[6:7], 0, v[108:109]
	v_lshl_add_u64 v[98:99], v[8:9], 0, v[110:111]
	global_load_dwordx4 v[60:63], v[112:113], off nt
	global_load_dwordx4 v[64:67], v[108:109], off offset:16
	global_load_dwordx4 v[68:71], v[108:109], off
	v_cvt_pk_bf16_f32 v116, v40, v41
	v_cvt_pk_bf16_f32 v117, v42, v43
	v_cvt_pk_bf16_f32 v118, v44, v45
	v_cvt_pk_bf16_f32 v119, v46, v47
	global_store_dwordx4 v[96:97], v[116:119], off
	s_waitcnt vmcnt(5)
	v_lshlrev_b32_e32 v114, 16, v48
	v_and_b32_e32 v115, 0xffff0000, v48
	v_pk_fma_f32 v[40:41], v[40:41], v[56:57], v[114:115]
	v_lshlrev_b32_e32 v114, 16, v49
	v_and_b32_e32 v115, 0xffff0000, v49
	v_pk_fma_f32 v[42:43], v[42:43], v[58:59], v[114:115]
	v_lshlrev_b32_e32 v114, 16, v50
	v_and_b32_e32 v115, 0xffff0000, v50
	v_pk_fma_f32 v[44:45], v[44:45], v[52:53], v[114:115]
	v_lshlrev_b32_e32 v114, 16, v51
	v_and_b32_e32 v115, 0xffff0000, v51
	v_pk_fma_f32 v[46:47], v[46:47], v[54:55], v[114:115]
	v_mov_b32_e32 v106, 5
	v_cndmask_b32_e64 v106, v106, 26, vcc
	v_lshl_add_u64 v[108:109], v[2:3], 0, v[106:107]
	v_lshlrev_b64 v[110:111], 15, v[108:109]
	v_lshlrev_b64 v[108:109], 9, v[108:109]
	v_lshl_add_u64 v[112:113], v[4:5], 0, v[110:111]
	v_lshl_add_u64 v[108:109], v[6:7], 0, v[108:109]
	v_lshl_add_u64 v[96:97], v[8:9], 0, v[110:111]
	global_load_dwordx4 v[48:51], v[112:113], off nt
	global_load_dwordx4 v[52:55], v[108:109], off offset:16
	global_load_dwordx4 v[56:59], v[108:109], off
	v_cvt_pk_bf16_f32 v116, v40, v41
	v_cvt_pk_bf16_f32 v117, v42, v43
	v_cvt_pk_bf16_f32 v118, v44, v45
	v_cvt_pk_bf16_f32 v119, v46, v47
	global_store_dwordx4 v[98:99], v[116:119], off
	s_waitcnt vmcnt(5)
	v_lshlrev_b32_e32 v114, 16, v60
	v_and_b32_e32 v115, 0xffff0000, v60
	v_pk_fma_f32 v[40:41], v[40:41], v[68:69], v[114:115]
	v_lshlrev_b32_e32 v114, 16, v61
	v_and_b32_e32 v115, 0xffff0000, v61
	v_pk_fma_f32 v[42:43], v[42:43], v[70:71], v[114:115]
	v_lshlrev_b32_e32 v114, 16, v62
	v_and_b32_e32 v115, 0xffff0000, v62
	v_pk_fma_f32 v[44:45], v[44:45], v[64:65], v[114:115]
	v_lshlrev_b32_e32 v114, 16, v63
	v_and_b32_e32 v115, 0xffff0000, v63
	v_pk_fma_f32 v[46:47], v[46:47], v[66:67], v[114:115]
	v_mov_b32_e32 v106, 4
	v_cndmask_b32_e64 v106, v106, 27, vcc
	v_lshl_add_u64 v[108:109], v[2:3], 0, v[106:107]
	v_lshlrev_b64 v[110:111], 15, v[108:109]
	v_lshlrev_b64 v[108:109], 9, v[108:109]
	v_lshl_add_u64 v[112:113], v[4:5], 0, v[110:111]
	v_lshl_add_u64 v[108:109], v[6:7], 0, v[108:109]
	v_lshl_add_u64 v[98:99], v[8:9], 0, v[110:111]
	global_load_dwordx4 v[60:63], v[112:113], off nt
	global_load_dwordx4 v[64:67], v[108:109], off offset:16
	global_load_dwordx4 v[68:71], v[108:109], off
	v_cvt_pk_bf16_f32 v116, v40, v41
	v_cvt_pk_bf16_f32 v117, v42, v43
	v_cvt_pk_bf16_f32 v118, v44, v45
	v_cvt_pk_bf16_f32 v119, v46, v47
	global_store_dwordx4 v[96:97], v[116:119], off
	s_waitcnt vmcnt(5)
	v_lshlrev_b32_e32 v114, 16, v48
	v_and_b32_e32 v115, 0xffff0000, v48
	v_pk_fma_f32 v[40:41], v[40:41], v[56:57], v[114:115]
	v_lshlrev_b32_e32 v114, 16, v49
	v_and_b32_e32 v115, 0xffff0000, v49
	v_pk_fma_f32 v[42:43], v[42:43], v[58:59], v[114:115]
	v_lshlrev_b32_e32 v114, 16, v50
	v_and_b32_e32 v115, 0xffff0000, v50
	v_pk_fma_f32 v[44:45], v[44:45], v[52:53], v[114:115]
	v_lshlrev_b32_e32 v114, 16, v51
	v_and_b32_e32 v115, 0xffff0000, v51
	v_pk_fma_f32 v[46:47], v[46:47], v[54:55], v[114:115]
	v_mov_b32_e32 v106, 3
	v_cndmask_b32_e64 v106, v106, 28, vcc
	v_lshl_add_u64 v[108:109], v[2:3], 0, v[106:107]
	v_lshlrev_b64 v[110:111], 15, v[108:109]
	v_lshlrev_b64 v[108:109], 9, v[108:109]
	v_lshl_add_u64 v[112:113], v[4:5], 0, v[110:111]
	v_lshl_add_u64 v[108:109], v[6:7], 0, v[108:109]
	v_lshl_add_u64 v[96:97], v[8:9], 0, v[110:111]
	global_load_dwordx4 v[48:51], v[112:113], off nt
	global_load_dwordx4 v[52:55], v[108:109], off offset:16
	global_load_dwordx4 v[56:59], v[108:109], off
	v_cvt_pk_bf16_f32 v116, v40, v41
	v_cvt_pk_bf16_f32 v117, v42, v43
	v_cvt_pk_bf16_f32 v118, v44, v45
	v_cvt_pk_bf16_f32 v119, v46, v47
	global_store_dwordx4 v[98:99], v[116:119], off
	s_waitcnt vmcnt(5)
; __device__ __forceinline__ unsigned cvt_pk_bf16(float lo, float hi) { const bf16x2_t r = __builtin_convertvector((f32x2_t){lo, hi}, bf16x2_t); return __builtin_bit_cast(unsigned, r); }
; __device__ __forceinline__ int tid_hidden() { int t = threadIdx.x; asm volatile("" : "+v"(t)); return t; }
; #define DEC WSP(float, W_DEC)
; __device__ __forceinline__ void c2_phase(const bf16_t* __restrict__ UT, const float* __restrict__ DEC, bf16_t* __restrict__ SIN, int G, int c) {
;     for (int w = c * 512 + tid_hidden(); w < 64 * 2048; w += G * 512) {
;         const int seq = w >> 11, e = (w >> 4) & 127, d8 = (w & 15) * 8, dir = seq >> 5;
;         float S[8];
; #pragma unroll
;         for (int k = 0; k < 8; ++k) S[k] = 0.f;
; #pragma unroll 4
;         for (int step = 0; step < 32; ++step) {
;             const int j = dir ? 31 - step : step;
;             const size_t idx = (size_t)seq * 32 + j;
;             const u32x4 u = __builtin_nontemporal_load((const u32x4*)(UT + idx * 16384 + e * 128 + d8));
;             const f32x4 dc0 = *(const f32x4*)(DEC + idx * 128 + d8), dc1 = *(const f32x4*)(DEC + idx * 128 + d8 + 4);
;             u32x4 o; o.x = cvt_pk_bf16(S[0], S[1]); o.y = cvt_pk_bf16(S[2], S[3]); o.z = cvt_pk_bf16(S[4], S[5]); o.w = cvt_pk_bf16(S[6], S[7]);
;             *(u32x4*)(SIN + idx * 16384 + e * 128 + d8) = o;
;             S[0] = dc0[0] * S[0] + __uint_as_float(u.x << 16); S[1] = dc0[1] * S[1] + __uint_as_float(u.x & 0xffff0000u);
;             S[2] = dc0[2] * S[2] + __uint_as_float(u.y << 16); S[3] = dc0[3] * S[3] + __uint_as_float(u.y & 0xffff0000u);
;             S[4] = dc1[0] * S[4] + __uint_as_float(u.z << 16); S[5] = dc1[1] * S[5] + __uint_as_float(u.z & 0xffff0000u);
;             S[6] = dc1[2] * S[6] + __uint_as_float(u.w << 16); S[7] = dc1[3] * S[7] + __uint_as_float(u.w & 0xffff0000u);
;         }
;     }
	v_lshlrev_b32_e32 v114, 16, v60
	v_and_b32_e32 v115, 0xffff0000, v60
	v_pk_fma_f32 v[40:41], v[40:41], v[68:69], v[114:115]
	v_lshlrev_b32_e32 v114, 16, v61
	v_and_b32_e32 v115, 0xffff0000, v61
	v_pk_fma_f32 v[42:43], v[42:43], v[70:71], v[114:115]
	v_lshlrev_b32_e32 v114, 16, v62
	v_and_b32_e32 v115, 0xffff0000, v62
	v_pk_fma_f32 v[44:45], v[44:45], v[64:65], v[114:115]
	v_lshlrev_b32_e32 v114, 16, v63
	v_and_b32_e32 v115, 0xffff0000, v63
	v_pk_fma_f32 v[46:47], v[46:47], v[66:67], v[114:115]
	v_mov_b32_e32 v106, 2
	v_cndmask_b32_e64 v106, v106, 29, vcc
	v_lshl_add_u64 v[108:109], v[2:3], 0, v[106:107]
	v_lshlrev_b64 v[110:111], 15, v[108:109]
	v_lshlrev_b64 v[108:109], 9, v[108:109]
	v_lshl_add_u64 v[112:113], v[4:5], 0, v[110:111]
	v_lshl_add_u64 v[108:109], v[6:7], 0, v[108:109]
	v_lshl_add_u64 v[98:99], v[8:9], 0, v[110:111]
	global_load_dwordx4 v[60:63], v[112:113], off nt
	global_load_dwordx4 v[64:67], v[108:109], off offset:16
	global_load_dwordx4 v[68:71], v[108:109], off
	v_cvt_pk_bf16_f32 v116, v40, v41
	v_cvt_pk_bf16_f32 v117, v42, v43
	v_cvt_pk_bf16_f32 v118, v44, v45
	v_cvt_pk_bf16_f32 v119, v46, v47
	global_store_dwordx4 v[96:97], v[116:119], off
	s_waitcnt vmcnt(5)
	v_lshlrev_b32_e32 v114, 16, v48
	v_and_b32_e32 v115, 0xffff0000, v48
	v_pk_fma_f32 v[40:41], v[40:41], v[56:57], v[114:115]
	v_lshlrev_b32_e32 v114, 16, v49
	v_and_b32_e32 v115, 0xffff0000, v49
	v_pk_fma_f32 v[42:43], v[42:43], v[58:59], v[114:115]
	v_lshlrev_b32_e32 v114, 16, v50
	v_and_b32_e32 v115, 0xffff0000, v50
	v_pk_fma_f32 v[44:45], v[44:45], v[52:53], v[114:115]
	v_lshlrev_b32_e32 v114, 16, v51
	v_and_b32_e32 v115, 0xffff0000, v51
	v_pk_fma_f32 v[46:47], v[46:47], v[54:55], v[114:115]
	v_mov_b32_e32 v106, 1
	v_cndmask_b32_e64 v106, v106, 30, vcc
	v_lshl_add_u64 v[108:109], v[2:3], 0, v[106:107]
	v_lshlrev_b64 v[110:111], 15, v[108:109]
	v_lshlrev_b64 v[108:109], 9, v[108:109]
	v_lshl_add_u64 v[112:113], v[4:5], 0, v[110:111]
	v_lshl_add_u64 v[108:109], v[6:7], 0, v[108:109]
	v_lshl_add_u64 v[96:97], v[8:9], 0, v[110:111]
	global_load_dwordx4 v[48:51], v[112:113], off nt
	global_load_dwordx4 v[52:55], v[108:109], off offset:16
	global_load_dwordx4 v[56:59], v[108:109], off
	v_cvt_pk_bf16_f32 v116, v40, v41
	v_cvt_pk_bf16_f32 v117, v42, v43
	v_cvt_pk_bf16_f32 v118, v44, v45
	v_cvt_pk_bf16_f32 v119, v46, v47
	global_store_dwordx4 v[98:99], v[116:119], off
	s_waitcnt vmcnt(5)
	v_lshlrev_b32_e32 v114, 16, v60
	v_and_b32_e32 v115, 0xffff0000, v60
	v_pk_fma_f32 v[40:41], v[40:41], v[68:69], v[114:115]
	v_lshlrev_b32_e32 v114, 16, v61
	v_and_b32_e32 v115, 0xffff0000, v61
	v_pk_fma_f32 v[42:43], v[42:43], v[70:71], v[114:115]
	v_lshlrev_b32_e32 v114, 16, v62
	v_and_b32_e32 v115, 0xffff0000, v62
	v_pk_fma_f32 v[44:45], v[44:45], v[64:65], v[114:115]
	v_lshlrev_b32_e32 v114, 16, v63
	v_and_b32_e32 v115, 0xffff0000, v63
	v_pk_fma_f32 v[46:47], v[46:47], v[66:67], v[114:115]
	v_mov_b32_e32 v106, 0
	v_cndmask_b32_e64 v106, v106, 31, vcc
	v_lshl_add_u64 v[108:109], v[2:3], 0, v[106:107]
	v_lshlrev_b64 v[110:111], 15, v[108:109]
	v_lshlrev_b64 v[108:109], 9, v[108:109]
	v_lshl_add_u64 v[112:113], v[4:5], 0, v[110:111]
	v_lshl_add_u64 v[108:109], v[6:7], 0, v[108:109]
	v_lshl_add_u64 v[98:99], v[8:9], 0, v[110:111]
	global_load_dwordx4 v[60:63], v[112:113], off nt
	global_load_dwordx4 v[64:67], v[108:109], off offset:16
	global_load_dwordx4 v[68:71], v[108:109], off
	v_cvt_pk_bf16_f32 v116, v40, v41
	v_cvt_pk_bf16_f32 v117, v42, v43
	v_cvt_pk_bf16_f32 v118, v44, v45
	v_cvt_pk_bf16_f32 v119, v46, v47
	global_store_dwordx4 v[96:97], v[116:119], off
	s_waitcnt vmcnt(5)
	v_lshlrev_b32_e32 v114, 16, v48
	v_and_b32_e32 v115, 0xffff0000, v48
	v_pk_fma_f32 v[40:41], v[40:41], v[56:57], v[114:115]
	v_lshlrev_b32_e32 v114, 16, v49
	v_and_b32_e32 v115, 0xffff0000, v49
	v_pk_fma_f32 v[42:43], v[42:43], v[58:59], v[114:115]
	v_lshlrev_b32_e32 v114, 16, v50
	v_and_b32_e32 v115, 0xffff0000, v50
	v_pk_fma_f32 v[44:45], v[44:45], v[52:53], v[114:115]
	v_lshlrev_b32_e32 v114, 16, v51
	v_and_b32_e32 v115, 0xffff0000, v51
	v_pk_fma_f32 v[46:47], v[46:47], v[54:55], v[114:115]
	v_cvt_pk_bf16_f32 v116, v40, v41
	v_cvt_pk_bf16_f32 v117, v42, v43
	v_cvt_pk_bf16_f32 v118, v44, v45
	v_cvt_pk_bf16_f32 v119, v46, v47
	global_store_dwordx4 v[98:99], v[116:119], off
	s_waitcnt vmcnt(2)
	v_lshlrev_b32_e32 v114, 16, v60
	v_and_b32_e32 v115, 0xffff0000, v60
	v_pk_fma_f32 v[40:41], v[40:41], v[68:69], v[114:115]
	v_lshlrev_b32_e32 v114, 16, v61
	v_and_b32_e32 v115, 0xffff0000, v61
	v_pk_fma_f32 v[42:43], v[42:43], v[70:71], v[114:115]
	v_lshlrev_b32_e32 v114, 16, v62
	v_and_b32_e32 v115, 0xffff0000, v62
	v_pk_fma_f32 v[44:45], v[44:45], v[64:65], v[114:115]
	v_lshlrev_b32_e32 v114, 16, v63
	v_and_b32_e32 v115, 0xffff0000, v63
	v_pk_fma_f32 v[46:47], v[46:47], v[66:67], v[114:115]
	v_add_u32_e32 v20, s11, v20
	s_mov_b32 s12, 0x1ffff
	v_cmp_lt_i32_e32 vcc, s12, v20
	s_or_b64 s[8:9], vcc, s[8:9]
	s_andn2_b64 exec, exec, s[8:9]
	s_cbranch_execnz .LBB0_1025
